# compact shared selection-mask block loop (lane-compare accumulate), second measure
# speedup vs baseline: 1.0042x; 1.0018x over previous
.Lmg_body:
	s_and_b32 s15, s14, 3
	s_lshl_b32 s15, s15, 4
	v_subrev_u32_e32 v43, s15, v74
	s_cmp_lg_u32 s12, 0
	s_cbranch_scc1 .Lmg_simple
	s_lshl_b32 s16, s14, 8
	v_or_b32_e32 v27, s16, v76
	v_cmp_eq_u32_e32 vcc, v8, v22
	v_cmp_gt_u32_e64 s[10:11], v8, v22
	v_add_u32_e32 v36, 0, v27
	v_lshrrev_b64 v[34:35], v2, vcc
	v_and_b32_e32 v37, 0xffff, v34
	v_and_b32_e32 v34, v34, v0
	v_bcnt_u32_b32 v34, v34, v26
	v_cmp_lt_i32_e64 s[16:17], v34, v23
	v_cmp_le_i32_e64 s[18:19], v36, v75
	v_bcnt_u32_b32 v26, v37, v26
	s_and_b64 s[4:5], vcc, s[16:17]
	s_or_b64 s[4:5], s[10:11], s[4:5]
	s_and_b64 s[4:5], s[4:5], s[18:19]
	v_cmp_eq_u32_e64 s[36:37], 0, v43
	v_mov_b32_e32 v34, s4
	v_mov_b32_e32 v35, s5
	v_cndmask_b32_e64 v6, v6, v34, s[36:37]
	v_cndmask_b32_e64 v7, v7, v35, s[36:37]
	v_cmp_eq_u32_e32 vcc, v9, v22
	v_cmp_gt_u32_e64 s[10:11], v9, v22
	v_add_u32_e32 v36, 16, v27
	v_lshrrev_b64 v[34:35], v2, vcc
	v_and_b32_e32 v37, 0xffff, v34
	v_and_b32_e32 v34, v34, v0
	v_bcnt_u32_b32 v34, v34, v26
	v_cmp_lt_i32_e64 s[16:17], v34, v23
	v_cmp_le_i32_e64 s[18:19], v36, v75
	v_bcnt_u32_b32 v26, v37, v26
	s_and_b64 s[4:5], vcc, s[16:17]
	s_or_b64 s[4:5], s[10:11], s[4:5]
	s_and_b64 s[4:5], s[4:5], s[18:19]
	v_cmp_eq_u32_e64 s[36:37], 1, v43
	v_mov_b32_e32 v34, s4
	v_mov_b32_e32 v35, s5
	v_cndmask_b32_e64 v6, v6, v34, s[36:37]
	v_cndmask_b32_e64 v7, v7, v35, s[36:37]
	v_cmp_eq_u32_e32 vcc, v10, v22
	v_cmp_gt_u32_e64 s[10:11], v10, v22
	v_add_u32_e32 v36, 32, v27
	v_lshrrev_b64 v[34:35], v2, vcc
	v_and_b32_e32 v37, 0xffff, v34
	v_and_b32_e32 v34, v34, v0
	v_bcnt_u32_b32 v34, v34, v26
	v_cmp_lt_i32_e64 s[16:17], v34, v23
	v_cmp_le_i32_e64 s[18:19], v36, v75
	v_bcnt_u32_b32 v26, v37, v26
	s_and_b64 s[4:5], vcc, s[16:17]
	s_or_b64 s[4:5], s[10:11], s[4:5]
	s_and_b64 s[4:5], s[4:5], s[18:19]
	v_cmp_eq_u32_e64 s[36:37], 2, v43
	v_mov_b32_e32 v34, s4
	v_mov_b32_e32 v35, s5
	v_cndmask_b32_e64 v6, v6, v34, s[36:37]
	v_cndmask_b32_e64 v7, v7, v35, s[36:37]
	v_cmp_eq_u32_e32 vcc, v11, v22
	v_cmp_gt_u32_e64 s[10:11], v11, v22
	v_add_u32_e32 v36, 48, v27
	v_lshrrev_b64 v[34:35], v2, vcc
	v_and_b32_e32 v37, 0xffff, v34
	v_and_b32_e32 v34, v34, v0
	v_bcnt_u32_b32 v34, v34, v26
	v_cmp_lt_i32_e64 s[16:17], v34, v23
	v_cmp_le_i32_e64 s[18:19], v36, v75
	v_bcnt_u32_b32 v26, v37, v26
	s_and_b64 s[4:5], vcc, s[16:17]
	s_or_b64 s[4:5], s[10:11], s[4:5]
	s_and_b64 s[4:5], s[4:5], s[18:19]
	v_cmp_eq_u32_e64 s[36:37], 3, v43
	v_mov_b32_e32 v34, s4
	v_mov_b32_e32 v35, s5
	v_cndmask_b32_e64 v6, v6, v34, s[36:37]
	v_cndmask_b32_e64 v7, v7, v35, s[36:37]
	v_cmp_eq_u32_e32 vcc, v12, v22
	v_cmp_gt_u32_e64 s[10:11], v12, v22
	v_add_u32_e32 v36, 64, v27
	v_lshrrev_b64 v[34:35], v2, vcc
	v_and_b32_e32 v37, 0xffff, v34
	v_and_b32_e32 v34, v34, v0
	v_bcnt_u32_b32 v34, v34, v26
	v_cmp_lt_i32_e64 s[16:17], v34, v23
	v_cmp_le_i32_e64 s[18:19], v36, v75
	v_bcnt_u32_b32 v26, v37, v26
	s_and_b64 s[4:5], vcc, s[16:17]
	s_or_b64 s[4:5], s[10:11], s[4:5]
	s_and_b64 s[4:5], s[4:5], s[18:19]
	v_cmp_eq_u32_e64 s[36:37], 4, v43
	v_mov_b32_e32 v34, s4
	v_mov_b32_e32 v35, s5
	v_cndmask_b32_e64 v6, v6, v34, s[36:37]
	v_cndmask_b32_e64 v7, v7, v35, s[36:37]
	v_cmp_eq_u32_e32 vcc, v13, v22
	v_cmp_gt_u32_e64 s[10:11], v13, v22
	v_add_u32_e32 v36, 80, v27
	v_lshrrev_b64 v[34:35], v2, vcc
	v_and_b32_e32 v37, 0xffff, v34
	v_and_b32_e32 v34, v34, v0
	v_bcnt_u32_b32 v34, v34, v26
	v_cmp_lt_i32_e64 s[16:17], v34, v23
	v_cmp_le_i32_e64 s[18:19], v36, v75
	v_bcnt_u32_b32 v26, v37, v26
	s_and_b64 s[4:5], vcc, s[16:17]
	s_or_b64 s[4:5], s[10:11], s[4:5]
	s_and_b64 s[4:5], s[4:5], s[18:19]
	v_cmp_eq_u32_e64 s[36:37], 5, v43
	v_mov_b32_e32 v34, s4
	v_mov_b32_e32 v35, s5
	v_cndmask_b32_e64 v6, v6, v34, s[36:37]
	v_cndmask_b32_e64 v7, v7, v35, s[36:37]
	v_cmp_eq_u32_e32 vcc, v14, v22
	v_cmp_gt_u32_e64 s[10:11], v14, v22
	v_add_u32_e32 v36, 96, v27
	v_lshrrev_b64 v[34:35], v2, vcc
	v_and_b32_e32 v37, 0xffff, v34
	v_and_b32_e32 v34, v34, v0
	v_bcnt_u32_b32 v34, v34, v26
	v_cmp_lt_i32_e64 s[16:17], v34, v23
	v_cmp_le_i32_e64 s[18:19], v36, v75
	v_bcnt_u32_b32 v26, v37, v26
	s_and_b64 s[4:5], vcc, s[16:17]
	s_or_b64 s[4:5], s[10:11], s[4:5]
	s_and_b64 s[4:5], s[4:5], s[18:19]
	v_cmp_eq_u32_e64 s[36:37], 6, v43
	v_mov_b32_e32 v34, s4
	v_mov_b32_e32 v35, s5
	v_cndmask_b32_e64 v6, v6, v34, s[36:37]
	v_cndmask_b32_e64 v7, v7, v35, s[36:37]
	v_cmp_eq_u32_e32 vcc, v15, v22
	v_cmp_gt_u32_e64 s[10:11], v15, v22
	v_add_u32_e32 v36, 112, v27
	v_lshrrev_b64 v[34:35], v2, vcc
	v_and_b32_e32 v37, 0xffff, v34
	v_and_b32_e32 v34, v34, v0
	v_bcnt_u32_b32 v34, v34, v26
	v_cmp_lt_i32_e64 s[16:17], v34, v23
	v_cmp_le_i32_e64 s[18:19], v36, v75
	v_bcnt_u32_b32 v26, v37, v26
	s_and_b64 s[4:5], vcc, s[16:17]
	s_or_b64 s[4:5], s[10:11], s[4:5]
	s_and_b64 s[4:5], s[4:5], s[18:19]
	v_cmp_eq_u32_e64 s[36:37], 7, v43
	v_mov_b32_e32 v34, s4
	v_mov_b32_e32 v35, s5
	v_cndmask_b32_e64 v6, v6, v34, s[36:37]
	v_cndmask_b32_e64 v7, v7, v35, s[36:37]
	v_cmp_eq_u32_e32 vcc, v16, v22
	v_cmp_gt_u32_e64 s[10:11], v16, v22
	v_add_u32_e32 v36, 128, v27
	v_lshrrev_b64 v[34:35], v2, vcc
	v_and_b32_e32 v37, 0xffff, v34
	v_and_b32_e32 v34, v34, v0
	v_bcnt_u32_b32 v34, v34, v26
	v_cmp_lt_i32_e64 s[16:17], v34, v23
	v_cmp_le_i32_e64 s[18:19], v36, v75
	v_bcnt_u32_b32 v26, v37, v26
	s_and_b64 s[4:5], vcc, s[16:17]
	s_or_b64 s[4:5], s[10:11], s[4:5]
	s_and_b64 s[4:5], s[4:5], s[18:19]
	v_cmp_eq_u32_e64 s[36:37], 8, v43
	v_mov_b32_e32 v34, s4
	v_mov_b32_e32 v35, s5
	v_cndmask_b32_e64 v6, v6, v34, s[36:37]
	v_cndmask_b32_e64 v7, v7, v35, s[36:37]
	v_cmp_eq_u32_e32 vcc, v17, v22
	v_cmp_gt_u32_e64 s[10:11], v17, v22
	v_add_u32_e32 v36, 144, v27
	v_lshrrev_b64 v[34:35], v2, vcc
	v_and_b32_e32 v37, 0xffff, v34
	v_and_b32_e32 v34, v34, v0
	v_bcnt_u32_b32 v34, v34, v26
	v_cmp_lt_i32_e64 s[16:17], v34, v23
	v_cmp_le_i32_e64 s[18:19], v36, v75
	v_bcnt_u32_b32 v26, v37, v26
	s_and_b64 s[4:5], vcc, s[16:17]
	s_or_b64 s[4:5], s[10:11], s[4:5]
	s_and_b64 s[4:5], s[4:5], s[18:19]
	v_cmp_eq_u32_e64 s[36:37], 9, v43
	v_mov_b32_e32 v34, s4
	v_mov_b32_e32 v35, s5
	v_cndmask_b32_e64 v6, v6, v34, s[36:37]
	v_cndmask_b32_e64 v7, v7, v35, s[36:37]
	v_cmp_eq_u32_e32 vcc, v18, v22
	v_cmp_gt_u32_e64 s[10:11], v18, v22
	v_add_u32_e32 v36, 160, v27
	v_lshrrev_b64 v[34:35], v2, vcc
	v_and_b32_e32 v37, 0xffff, v34
	v_and_b32_e32 v34, v34, v0
	v_bcnt_u32_b32 v34, v34, v26
	v_cmp_lt_i32_e64 s[16:17], v34, v23
	v_cmp_le_i32_e64 s[18:19], v36, v75
	v_bcnt_u32_b32 v26, v37, v26
	s_and_b64 s[4:5], vcc, s[16:17]
	s_or_b64 s[4:5], s[10:11], s[4:5]
	s_and_b64 s[4:5], s[4:5], s[18:19]
	v_cmp_eq_u32_e64 s[36:37], 10, v43
	v_mov_b32_e32 v34, s4
	v_mov_b32_e32 v35, s5
	v_cndmask_b32_e64 v6, v6, v34, s[36:37]
	v_cndmask_b32_e64 v7, v7, v35, s[36:37]
	v_cmp_eq_u32_e32 vcc, v19, v22
	v_cmp_gt_u32_e64 s[10:11], v19, v22
	v_add_u32_e32 v36, 176, v27
	v_lshrrev_b64 v[34:35], v2, vcc
	v_and_b32_e32 v37, 0xffff, v34
	v_and_b32_e32 v34, v34, v0
	v_bcnt_u32_b32 v34, v34, v26
	v_cmp_lt_i32_e64 s[16:17], v34, v23
	v_cmp_le_i32_e64 s[18:19], v36, v75
	v_bcnt_u32_b32 v26, v37, v26
	s_and_b64 s[4:5], vcc, s[16:17]
	s_or_b64 s[4:5], s[10:11], s[4:5]
	s_and_b64 s[4:5], s[4:5], s[18:19]
	v_cmp_eq_u32_e64 s[36:37], 11, v43
	v_mov_b32_e32 v34, s4
	v_mov_b32_e32 v35, s5
	v_cndmask_b32_e64 v6, v6, v34, s[36:37]
	v_cndmask_b32_e64 v7, v7, v35, s[36:37]
	v_cmp_eq_u32_e32 vcc, v28, v22
	v_cmp_gt_u32_e64 s[10:11], v28, v22
	v_add_u32_e32 v36, 192, v27
	v_lshrrev_b64 v[34:35], v2, vcc
	v_and_b32_e32 v37, 0xffff, v34
	v_and_b32_e32 v34, v34, v0
	v_bcnt_u32_b32 v34, v34, v26
	v_cmp_lt_i32_e64 s[16:17], v34, v23
	v_cmp_le_i32_e64 s[18:19], v36, v75
	v_bcnt_u32_b32 v26, v37, v26
	s_and_b64 s[4:5], vcc, s[16:17]
	s_or_b64 s[4:5], s[10:11], s[4:5]
	s_and_b64 s[4:5], s[4:5], s[18:19]
	v_cmp_eq_u32_e64 s[36:37], 12, v43
	v_mov_b32_e32 v34, s4
	v_mov_b32_e32 v35, s5
	v_cndmask_b32_e64 v6, v6, v34, s[36:37]
	v_cndmask_b32_e64 v7, v7, v35, s[36:37]
	v_cmp_eq_u32_e32 vcc, v29, v22
	v_cmp_gt_u32_e64 s[10:11], v29, v22
	v_add_u32_e32 v36, 208, v27
	v_lshrrev_b64 v[34:35], v2, vcc
	v_and_b32_e32 v37, 0xffff, v34
	v_and_b32_e32 v34, v34, v0
	v_bcnt_u32_b32 v34, v34, v26
	v_cmp_lt_i32_e64 s[16:17], v34, v23
	v_cmp_le_i32_e64 s[18:19], v36, v75
	v_bcnt_u32_b32 v26, v37, v26
	s_and_b64 s[4:5], vcc, s[16:17]
	s_or_b64 s[4:5], s[10:11], s[4:5]
	s_and_b64 s[4:5], s[4:5], s[18:19]
	v_cmp_eq_u32_e64 s[36:37], 13, v43
	v_mov_b32_e32 v34, s4
	v_mov_b32_e32 v35, s5
	v_cndmask_b32_e64 v6, v6, v34, s[36:37]
	v_cndmask_b32_e64 v7, v7, v35, s[36:37]
	v_cmp_eq_u32_e32 vcc, v30, v22
	v_cmp_gt_u32_e64 s[10:11], v30, v22
	v_add_u32_e32 v36, 224, v27
	v_lshrrev_b64 v[34:35], v2, vcc
	v_and_b32_e32 v37, 0xffff, v34
	v_and_b32_e32 v34, v34, v0
	v_bcnt_u32_b32 v34, v34, v26
	v_cmp_lt_i32_e64 s[16:17], v34, v23
	v_cmp_le_i32_e64 s[18:19], v36, v75
	v_bcnt_u32_b32 v26, v37, v26
	s_and_b64 s[4:5], vcc, s[16:17]
	s_or_b64 s[4:5], s[10:11], s[4:5]
	s_and_b64 s[4:5], s[4:5], s[18:19]
	v_cmp_eq_u32_e64 s[36:37], 14, v43
	v_mov_b32_e32 v34, s4
	v_mov_b32_e32 v35, s5
	v_cndmask_b32_e64 v6, v6, v34, s[36:37]
	v_cndmask_b32_e64 v7, v7, v35, s[36:37]
	v_cmp_eq_u32_e32 vcc, v31, v22
	v_cmp_gt_u32_e64 s[10:11], v31, v22
	v_add_u32_e32 v36, 240, v27
	v_lshrrev_b64 v[34:35], v2, vcc
	v_and_b32_e32 v37, 0xffff, v34
	v_and_b32_e32 v34, v34, v0
	v_bcnt_u32_b32 v34, v34, v26
	v_cmp_lt_i32_e64 s[16:17], v34, v23
	v_cmp_le_i32_e64 s[18:19], v36, v75
	v_bcnt_u32_b32 v26, v37, v26
	s_and_b64 s[4:5], vcc, s[16:17]
	s_or_b64 s[4:5], s[10:11], s[4:5]
	s_and_b64 s[4:5], s[4:5], s[18:19]
	v_cmp_eq_u32_e64 s[36:37], 15, v43
	v_mov_b32_e32 v34, s4
	v_mov_b32_e32 v35, s5
	v_cndmask_b32_e64 v6, v6, v34, s[36:37]
	v_cndmask_b32_e64 v7, v7, v35, s[36:37]
	s_branch .Lmg_next
.Lmg_simple:
	v_cmp_ge_u32_e64 s[16:17], v8, v22
	v_cmp_ge_u32_e64 s[18:19], v9, v22
	v_cmp_ge_u32_e64 s[22:23], v10, v22
	v_cmp_ge_u32_e64 s[24:25], v11, v22
	v_cmp_ge_u32_e64 s[28:29], v12, v22
	v_cmp_ge_u32_e64 s[30:31], v13, v22
	v_cmp_ge_u32_e64 s[32:33], v14, v22
	v_cmp_ge_u32_e64 s[34:35], v15, v22
	v_cmp_eq_u32_e64 s[36:37], 0, v43
	v_mov_b32_e32 v34, s16
	v_mov_b32_e32 v35, s17
	v_cndmask_b32_e64 v6, v6, v34, s[36:37]
	v_cndmask_b32_e64 v7, v7, v35, s[36:37]
	v_cmp_eq_u32_e64 s[36:37], 1, v43
	v_mov_b32_e32 v34, s18
	v_mov_b32_e32 v35, s19
	v_cndmask_b32_e64 v6, v6, v34, s[36:37]
	v_cndmask_b32_e64 v7, v7, v35, s[36:37]
	v_cmp_eq_u32_e64 s[36:37], 2, v43
	v_mov_b32_e32 v34, s22
	v_mov_b32_e32 v35, s23
	v_cndmask_b32_e64 v6, v6, v34, s[36:37]
	v_cndmask_b32_e64 v7, v7, v35, s[36:37]
	v_cmp_eq_u32_e64 s[36:37], 3, v43
	v_mov_b32_e32 v34, s24
	v_mov_b32_e32 v35, s25
	v_cndmask_b32_e64 v6, v6, v34, s[36:37]
	v_cndmask_b32_e64 v7, v7, v35, s[36:37]
	v_cmp_eq_u32_e64 s[36:37], 4, v43
	v_mov_b32_e32 v34, s28
	v_mov_b32_e32 v35, s29
	v_cndmask_b32_e64 v6, v6, v34, s[36:37]
	v_cndmask_b32_e64 v7, v7, v35, s[36:37]
	v_cmp_eq_u32_e64 s[36:37], 5, v43
	v_mov_b32_e32 v34, s30
	v_mov_b32_e32 v35, s31
	v_cndmask_b32_e64 v6, v6, v34, s[36:37]
	v_cndmask_b32_e64 v7, v7, v35, s[36:37]
	v_cmp_eq_u32_e64 s[36:37], 6, v43
	v_mov_b32_e32 v34, s32
	v_mov_b32_e32 v35, s33
	v_cndmask_b32_e64 v6, v6, v34, s[36:37]
	v_cndmask_b32_e64 v7, v7, v35, s[36:37]
	v_cmp_eq_u32_e64 s[36:37], 7, v43
	v_mov_b32_e32 v34, s34
	v_mov_b32_e32 v35, s35
	v_cndmask_b32_e64 v6, v6, v34, s[36:37]
	v_cndmask_b32_e64 v7, v7, v35, s[36:37]
	v_cmp_ge_u32_e64 s[16:17], v16, v22
	v_cmp_ge_u32_e64 s[18:19], v17, v22
	v_cmp_ge_u32_e64 s[22:23], v18, v22
	v_cmp_ge_u32_e64 s[24:25], v19, v22
	v_cmp_ge_u32_e64 s[28:29], v28, v22
	v_cmp_ge_u32_e64 s[30:31], v29, v22
	v_cmp_ge_u32_e64 s[32:33], v30, v22
	v_cmp_ge_u32_e64 s[34:35], v31, v22
	v_cmp_eq_u32_e64 s[36:37], 8, v43
	v_mov_b32_e32 v34, s16
	v_mov_b32_e32 v35, s17
	v_cndmask_b32_e64 v6, v6, v34, s[36:37]
	v_cndmask_b32_e64 v7, v7, v35, s[36:37]
	v_cmp_eq_u32_e64 s[36:37], 9, v43
	v_mov_b32_e32 v34, s18
	v_mov_b32_e32 v35, s19
	v_cndmask_b32_e64 v6, v6, v34, s[36:37]
	v_cndmask_b32_e64 v7, v7, v35, s[36:37]
	v_cmp_eq_u32_e64 s[36:37], 10, v43
	v_mov_b32_e32 v34, s22
	v_mov_b32_e32 v35, s23
	v_cndmask_b32_e64 v6, v6, v34, s[36:37]
	v_cndmask_b32_e64 v7, v7, v35, s[36:37]
	v_cmp_eq_u32_e64 s[36:37], 11, v43
	v_mov_b32_e32 v34, s24
	v_mov_b32_e32 v35, s25
	v_cndmask_b32_e64 v6, v6, v34, s[36:37]
	v_cndmask_b32_e64 v7, v7, v35, s[36:37]
	v_cmp_eq_u32_e64 s[36:37], 12, v43
	v_mov_b32_e32 v34, s28
	v_mov_b32_e32 v35, s29
	v_cndmask_b32_e64 v6, v6, v34, s[36:37]
	v_cndmask_b32_e64 v7, v7, v35, s[36:37]
	v_cmp_eq_u32_e64 s[36:37], 13, v43
	v_mov_b32_e32 v34, s30
	v_mov_b32_e32 v35, s31
	v_cndmask_b32_e64 v6, v6, v34, s[36:37]
	v_cndmask_b32_e64 v7, v7, v35, s[36:37]
	v_cmp_eq_u32_e64 s[36:37], 14, v43
	v_mov_b32_e32 v34, s32
	v_mov_b32_e32 v35, s33
	v_cndmask_b32_e64 v6, v6, v34, s[36:37]
	v_cndmask_b32_e64 v7, v7, v35, s[36:37]
	v_cmp_eq_u32_e64 s[36:37], 15, v43
	v_mov_b32_e32 v34, s34
	v_mov_b32_e32 v35, s35
	v_cndmask_b32_e64 v6, v6, v34, s[36:37]
	v_cndmask_b32_e64 v7, v7, v35, s[36:37]
.Lmg_next:
	s_add_i32 s14, s14, 1
	s_cmp_lt_u32 s14, s13
	s_cbranch_scc1 .Lmg_blk
	s_cmp_gt_u32 s13, 4
	s_cbranch_scc1 .Lmg_done
	v_mov_b32_e32 v4, v6
	v_mov_b32_e32 v5, v7
	v_mov_b32_e32 v6, 0
	v_mov_b32_e32 v7, 0
